# P2a pass prologue: first two W tiles issued behind the list-index loads (spare registers, counted waits) instead of after the gather offsets were built; plus v12 rcp divisions
# baseline (speedup 1.0000x reference)
.LBB0_263:
	s_sub_i32 s7, s62, s64
	v_mov_b32_e32 v162, v0
	s_min_i32 s7, s7, 0x200
	s_add_i32 s8, s7, 0x7f
	v_readfirstlane_b32 s6, v162
	s_lshr_b32 s66, s8, 7
	s_ashr_i32 s8, s6, 2
	s_and_b32 s8, s8, -16
	s_mul_i32 s8, s8, s66
	s_add_i32 s8, s8, s64
	v_bfe_u32 v2, v162, 3, 3
	v_or_b32_e32 v10, s8, v2
	s_add_i32 s65, s7, s64
	v_mov_b32_e32 v11, s64
	v_cmp_gt_i32_e32 vcc, s65, v10
	v_or_b32_e32 v4, 8, v10
	v_add_u32_e32 v6, 16, v10
	v_cndmask_b32_e32 v2, v11, v10, vcc
	v_cmp_gt_i32_e32 vcc, s65, v4
	s_cmpk_gt_u32 s7, 0x80
	s_cselect_b64 s[46:47], -1, 0
	v_cndmask_b32_e32 v4, v11, v4, vcc
	v_cmp_gt_i32_e32 vcc, s65, v6
	s_and_b64 vcc, s[46:47], vcc
	v_add_u32_e32 v8, 24, v10
	v_cndmask_b32_e32 v6, v11, v6, vcc
	v_cmp_gt_i32_e32 vcc, s65, v8
	s_and_b64 vcc, s[46:47], vcc
	v_ashrrev_i32_e32 v3, 31, v2
	v_ashrrev_i32_e32 v7, 31, v6
	v_cndmask_b32_e32 v8, v11, v8, vcc
	v_lshl_add_u64 v[2:3], v[2:3], 2, s[24:25]
	v_ashrrev_i32_e32 v5, 31, v4
	v_lshl_add_u64 v[6:7], v[6:7], 2, s[24:25]
	v_ashrrev_i32_e32 v9, 31, v8
	v_lshl_add_u64 v[4:5], v[4:5], 2, s[24:25]
	v_lshl_add_u64 v[8:9], v[8:9], 2, s[24:25]
	global_load_dword v12, v[2:3], off
	global_load_dword v13, v[4:5], off
	s_nop 0
	global_load_dword v6, v[6:7], off
	s_nop 0
	global_load_dword v7, v[8:9], off
	v_add_u32_e32 v2, 32, v10
	s_cmpk_gt_u32 s7, 0x100
	s_cselect_b64 s[44:45], -1, 0
	v_cmp_gt_i32_e32 vcc, s65, v2
	s_and_b64 vcc, s[44:45], vcc
	v_add_u32_e32 v4, 40, v10
	v_cndmask_b32_e32 v2, v11, v2, vcc
	v_cmp_gt_i32_e32 vcc, s65, v4
	s_and_b64 vcc, s[44:45], vcc
	v_ashrrev_i32_e32 v3, 31, v2
	v_cndmask_b32_e32 v4, v11, v4, vcc
	v_lshl_add_u64 v[2:3], v[2:3], 2, s[24:25]
	v_ashrrev_i32_e32 v5, 31, v4
	v_lshl_add_u64 v[4:5], v[4:5], 2, s[24:25]
	global_load_dword v8, v[2:3], off
	global_load_dword v9, v[4:5], off
	v_add_u32_e32 v2, 48, v10
	s_cmpk_gt_u32 s7, 0x180
	s_cselect_b64 s[42:43], -1, 0
	v_cmp_gt_i32_e32 vcc, s65, v2
	s_and_b64 vcc, s[42:43], vcc
	v_add_u32_e32 v4, 56, v10
	v_cndmask_b32_e32 v2, v11, v2, vcc
	v_cmp_gt_i32_e32 vcc, s65, v4
	s_and_b64 vcc, s[42:43], vcc
	v_ashrrev_i32_e32 v3, 31, v2
	v_cndmask_b32_e32 v4, v11, v4, vcc
	v_lshl_add_u64 v[2:3], v[2:3], 2, s[24:25]
	v_ashrrev_i32_e32 v5, 31, v4
	v_lshl_add_u64 v[4:5], v[4:5], 2, s[24:25]
	global_load_dword v131, v[2:3], off
	global_load_dword v130, v[4:5], off
	v_and_b32_e32 v10, 31, v162
	v_and_b32_e32 v2, 7, v162
	v_bfe_u32 v3, v162, 4, 2
	v_cmp_gt_u32_e32 vcc, 16, v10
	v_bitop3_b32 v2, v3, v2, 4 bitop3:0x36
	v_ashrrev_i32_e32 v11, 5, v162
	v_cndmask_b32_e32 v15, v166, v167, vcc
	v_bitop3_b32 v14, v3, v162, 7 bitop3:0x78
	v_lshlrev_b32_e32 v132, 4, v2
	v_lshl_add_u32 v2, v10, 4, v15
	v_lshlrev_b32_e32 v133, 4, v14
	v_lshl_or_b32 v168, v11, 13, v2
	global_load_dwordx4 v[228:231], v168, s[22:23]
	global_load_dwordx4 v[232:235], v168, s[22:23] offset:2048
	global_load_dwordx4 v[236:239], v168, s[28:29]
	global_load_dwordx4 v[240:243], v168, s[28:29] offset:2048
	global_load_dwordx4 v[60:63], v168, s[30:31]
	global_load_dwordx4 v[64:67], v168, s[30:31] offset:2048
	global_load_dwordx4 v[68:71], v168, s[34:35]
	global_load_dwordx4 v[72:75], v168, s[34:35] offset:2048
	v_lshrrev_b32_e32 v5, 4, v162
	v_lshlrev_b32_e32 v3, 11, v3
	s_lshl_b32 s6, s6, 8
	s_and_b32 s6, s6, 0xffffc000
	v_and_b32_e32 v4, 15, v162
	s_add_i32 s67, s6, 0
	s_add_i32 s68, s67, 0x400
	s_mov_b64 s[6:7], -1
	s_mov_b64 s[8:9], 0
	s_cmp_lt_i32 s66, 2
	s_mov_b64 s[10:11], 0
	s_waitcnt vmcnt(15)
	v_lshlrev_b32_e32 v2, 8, v12
	v_and_or_b32 v169, v2, s60, v133
	s_waitcnt vmcnt(14)
	v_lshlrev_b32_e32 v2, 8, v13
	v_and_or_b32 v170, v2, s60, v132
	s_waitcnt vmcnt(13)
	v_lshlrev_b32_e32 v2, 8, v6
	s_waitcnt vmcnt(12)
	v_lshlrev_b32_e32 v6, 8, v7
	v_and_or_b32 v175, v6, s60, v132
	v_and_or_b32 v174, v2, s60, v133
	s_waitcnt vmcnt(11)
	v_lshlrev_b32_e32 v2, 8, v8
	s_waitcnt vmcnt(10)
	v_lshlrev_b32_e32 v6, 8, v9
	v_and_or_b32 v177, v6, s60, v132
	v_lshlrev_b32_e32 v6, 3, v162
	v_and_or_b32 v176, v2, s60, v133
	v_lshlrev_b32_e32 v2, 10, v11
	v_and_b32_e32 v6, 24, v6
	v_add3_u32 v173, s61, v2, v6
	v_bfe_u32 v2, v162, 2, 3
	v_bitop3_b32 v134, v2, v5, 4 bitop3:0x78
	v_bfe_u32 v2, v162, 2, 2
	v_lshlrev_b32_e32 v7, 8, v2
	v_add3_u32 v3, s61, v3, v7
	v_lshrrev_b32_e32 v7, 2, v162
	v_and_or_b32 v2, v7, 4, v2
	v_lshlrev_b32_e32 v2, 5, v2
	v_add3_u32 v171, v3, v6, v2
	v_bfe_u32 v3, v162, 1, 3
	v_bitop3_b32 v3, v5, v3, 3 bitop3:0x6c
	v_lshlrev_b32_e32 v2, 7, v4
	v_lshlrev_b32_e32 v3, 4, v3
	v_add3_u32 v172, s67, v2, v3
	s_cbranch_scc1 .LBB0_275
	s_cmp_gt_i32 s66, 2
	s_cbranch_scc0 .LBB0_269
	s_cmp_eq_u32 s66, 3
	s_mov_b64 s[10:11], -1
	s_cbranch_scc0 .LBB0_270
	s_mov_b32 s6, m0
	s_mov_b32 m0, s67
	s_nop 0
	global_load_lds_dwordx4 v169, s[18:19]
	s_mov_b32 m0, s6
	s_add_i32 s52, s67, 0x800
	s_mov_b32 s6, m0
	s_mov_b32 m0, s68
	s_nop 0
	global_load_lds_dwordx4 v170, s[18:19]
	s_mov_b32 m0, s6
	s_add_i32 s53, s67, 0xc00
	s_mov_b32 s6, m0
	s_mov_b32 m0, s52
	s_nop 0
	global_load_lds_dwordx4 v174, s[18:19]
	s_mov_b32 m0, s6
	s_add_i32 s69, s67, 0x1000
	s_mov_b32 s6, m0
	s_mov_b32 m0, s53
	s_nop 0
	global_load_lds_dwordx4 v175, s[18:19]
	s_mov_b32 m0, s6
	s_add_i32 s70, s67, 0x1400
	s_mov_b32 s6, m0
	s_mov_b32 m0, s69
	s_nop 0
	global_load_lds_dwordx4 v176, s[18:19]
	s_mov_b32 m0, s6
	v_mov_b32_e32 v26, 0
	s_mov_b32 s6, m0
	s_mov_b32 m0, s70
	s_nop 0
	global_load_lds_dwordx4 v177, s[18:19]
	s_mov_b32 m0, s6
	s_waitcnt vmcnt(6)
	v_mov_b32_e32 v106, v60
	v_mov_b32_e32 v107, v61
	v_mov_b32_e32 v108, v62
	v_mov_b32_e32 v109, v63
	v_mov_b32_e32 v102, v64
	v_mov_b32_e32 v103, v65
	v_mov_b32_e32 v104, v66
	v_mov_b32_e32 v105, v67
	v_mov_b32_e32 v110, v68
	v_mov_b32_e32 v111, v69
	v_mov_b32_e32 v112, v70
	v_mov_b32_e32 v113, v71
	v_mov_b32_e32 v98, v72
	v_mov_b32_e32 v99, v73
	v_mov_b32_e32 v100, v74
	v_mov_b32_e32 v101, v75
	v_xor_b32_e32 v139, 64, v172
	v_cvt_pk_bf16_f32 v2, v228, v229
	v_cvt_pk_bf16_f32 v3, v230, v231
	v_lshlrev_b32_e32 v4, 5, v134
	v_add_u32_e32 v135, v173, v4
	v_xor_b32_e32 v5, 32, v4
	ds_write_b64 v135, v[2:3]
	v_cvt_pk_bf16_f32 v2, v232, v233
	v_cvt_pk_bf16_f32 v3, v234, v235
	v_add_u32_e32 v136, v173, v5
	v_xor_b32_e32 v5, 64, v4
	ds_write_b64 v136, v[2:3] offset:256
	v_cvt_pk_bf16_f32 v2, v236, v237
	v_cvt_pk_bf16_f32 v3, v238, v239
	v_add_u32_e32 v137, v173, v5
	v_xor_b32_e32 v4, 0x60, v4
	ds_write_b64 v137, v[2:3] offset:512
	v_cvt_pk_bf16_f32 v2, v240, v241
	v_cvt_pk_bf16_f32 v3, v242, v243
	v_add_u32_e32 v138, v173, v4
	ds_write_b64 v138, v[2:3] offset:768
	global_load_dwordx4 v[122:125], v168, s[38:39]
	global_load_dwordx4 v[118:121], v168, s[38:39] offset:2048
	global_load_dwordx4 v[126:129], v168, s[40:41]
	global_load_dwordx4 v[114:117], v168, s[40:41] offset:2048
	s_waitcnt lgkmcnt(0)
	s_barrier
	v_add_u32_e32 v2, 0x2000, v172
	s_add_i32 s71, s67, 0x2000
	v_xor_b32_e32 v140, 64, v2
	v_xor_b32_e32 v141, 32, v171
	v_xor_b32_e32 v142, 64, v171
	v_xor_b32_e32 v143, 0x60, v171
	v_xor_b32_e32 v144, 0x80, v171
	v_xor_b32_e32 v145, 0xa0, v171
	v_xor_b32_e32 v146, 0xc0, v171
	s_add_i32 s72, s67, 0x2400
	v_xor_b32_e32 v147, 0xe0, v171
	s_add_i32 s73, s67, 0x2800
	s_add_i32 s74, s67, 0x2c00
	s_add_i32 s75, s67, 0x3000
	s_add_i32 s76, s67, 0x3400
	s_mov_b32 s50, 0
	s_mov_b64 s[10:11], 0
	v_mov_b32_e32 v27, v26
	v_mov_b32_e32 v28, v26
	v_mov_b32_e32 v29, v26
	v_mov_b32_e32 v2, v26
	v_mov_b32_e32 v3, v26
	v_mov_b32_e32 v4, v26
	v_mov_b32_e32 v5, v26
	v_mov_b32_e32 v10, v26
	v_mov_b32_e32 v11, v26
	v_mov_b32_e32 v12, v26
	v_mov_b32_e32 v13, v26
	v_mov_b32_e32 v50, v26
	v_mov_b32_e32 v51, v26
	v_mov_b32_e32 v52, v26
	v_mov_b32_e32 v53, v26
	v_mov_b32_e32 v14, v26
	v_mov_b32_e32 v15, v26
	v_mov_b32_e32 v16, v26
	v_mov_b32_e32 v17, v26
	v_mov_b32_e32 v30, v26
	v_mov_b32_e32 v31, v26
	v_mov_b32_e32 v32, v26
	v_mov_b32_e32 v33, v26
	v_mov_b32_e32 v66, v26
	v_mov_b32_e32 v67, v26
	v_mov_b32_e32 v68, v26
	v_mov_b32_e32 v69, v26
	v_mov_b32_e32 v34, v26
	v_mov_b32_e32 v35, v26
	v_mov_b32_e32 v36, v26
	v_mov_b32_e32 v37, v26
	v_mov_b32_e32 v62, v26
	v_mov_b32_e32 v63, v26
	v_mov_b32_e32 v64, v26
	v_mov_b32_e32 v65, v26
	v_mov_b32_e32 v82, v26
	v_mov_b32_e32 v83, v26
	v_mov_b32_e32 v84, v26
	v_mov_b32_e32 v85, v26
	v_mov_b32_e32 v54, v26
	v_mov_b32_e32 v55, v26
	v_mov_b32_e32 v56, v26
	v_mov_b32_e32 v57, v26
	v_mov_b32_e32 v86, v26
	v_mov_b32_e32 v87, v26
	v_mov_b32_e32 v88, v26
	v_mov_b32_e32 v89, v26
	v_mov_b32_e32 v22, v26
	v_mov_b32_e32 v23, v26
	v_mov_b32_e32 v24, v26
	v_mov_b32_e32 v25, v26
	v_mov_b32_e32 v6, v26
	v_mov_b32_e32 v7, v26
	v_mov_b32_e32 v8, v26
	v_mov_b32_e32 v9, v26
	v_mov_b32_e32 v42, v26
	v_mov_b32_e32 v43, v26
	v_mov_b32_e32 v44, v26
	v_mov_b32_e32 v45, v26
	v_mov_b32_e32 v38, v26
	v_mov_b32_e32 v39, v26
	v_mov_b32_e32 v40, v26
	v_mov_b32_e32 v41, v26
	v_mov_b32_e32 v18, v26
	v_mov_b32_e32 v19, v26
	v_mov_b32_e32 v20, v26
	v_mov_b32_e32 v21, v26
	v_mov_b32_e32 v70, v26
	v_mov_b32_e32 v71, v26
	v_mov_b32_e32 v72, v26
	v_mov_b32_e32 v73, v26
	v_mov_b32_e32 v58, v26
	v_mov_b32_e32 v59, v26
	v_mov_b32_e32 v60, v26
	v_mov_b32_e32 v61, v26
	v_mov_b32_e32 v46, v26
	v_mov_b32_e32 v47, v26
	v_mov_b32_e32 v48, v26
	v_mov_b32_e32 v49, v26
	v_mov_b32_e32 v90, v26
	v_mov_b32_e32 v91, v26
	v_mov_b32_e32 v92, v26
	v_mov_b32_e32 v93, v26
	v_mov_b32_e32 v78, v26
	v_mov_b32_e32 v79, v26
	v_mov_b32_e32 v80, v26
	v_mov_b32_e32 v81, v26
	v_mov_b32_e32 v74, v26
	v_mov_b32_e32 v75, v26
	v_mov_b32_e32 v76, v26
	v_mov_b32_e32 v77, v26
	v_mov_b32_e32 v94, v26
	v_mov_b32_e32 v95, v26
	v_mov_b32_e32 v96, v26
	v_mov_b32_e32 v97, v26

.LBB0_271:
	s_mov_b32 s6, m0
	s_mov_b32 m0, s67
	s_nop 0
	global_load_lds_dwordx4 v169, s[18:19]
	s_mov_b32 m0, s6
	s_add_i32 s69, s67, 0x800
	s_mov_b32 s6, m0
	s_mov_b32 m0, s68
	s_nop 0
	global_load_lds_dwordx4 v170, s[18:19]
	s_mov_b32 m0, s6
	s_add_i32 s70, s67, 0xc00
	s_mov_b32 s6, m0
	s_mov_b32 m0, s69
	s_nop 0
	global_load_lds_dwordx4 v174, s[18:19]
	s_mov_b32 m0, s6
	v_xor_b32_e32 v102, 64, v172
	s_mov_b32 s6, m0
	s_mov_b32 m0, s70
	s_nop 0
	global_load_lds_dwordx4 v175, s[18:19]
	s_mov_b32 m0, s6
	s_waitcnt vmcnt(4)
	v_mov_b32_e32 v38, v60
	v_mov_b32_e32 v39, v61
	v_mov_b32_e32 v40, v62
	v_mov_b32_e32 v41, v63
	v_mov_b32_e32 v26, v64
	v_mov_b32_e32 v27, v65
	v_mov_b32_e32 v28, v66
	v_mov_b32_e32 v29, v67
	v_mov_b32_e32 v50, v68
	v_mov_b32_e32 v51, v69
	v_mov_b32_e32 v52, v70
	v_mov_b32_e32 v53, v71
	v_mov_b32_e32 v22, v72
	v_mov_b32_e32 v23, v73
	v_mov_b32_e32 v24, v74
	v_mov_b32_e32 v25, v75
	s_add_i32 s71, s67, 0x2000
	v_cvt_pk_bf16_f32 v2, v228, v229
	v_cvt_pk_bf16_f32 v3, v230, v231
	v_lshlrev_b32_e32 v4, 5, v134
	v_add_u32_e32 v98, v173, v4
	v_xor_b32_e32 v5, 32, v4
	ds_write_b64 v98, v[2:3]
	v_cvt_pk_bf16_f32 v2, v232, v233
	v_cvt_pk_bf16_f32 v3, v234, v235
	v_add_u32_e32 v99, v173, v5
	v_xor_b32_e32 v5, 64, v4
	ds_write_b64 v99, v[2:3] offset:256
	v_cvt_pk_bf16_f32 v2, v236, v237
	v_cvt_pk_bf16_f32 v3, v238, v239
	v_add_u32_e32 v100, v173, v5
	v_xor_b32_e32 v4, 0x60, v4
	ds_write_b64 v100, v[2:3] offset:512
	v_cvt_pk_bf16_f32 v2, v240, v241
	v_cvt_pk_bf16_f32 v3, v242, v243
	v_add_u32_e32 v101, v173, v4
	ds_write_b64 v101, v[2:3] offset:768
	global_load_dwordx4 v[78:81], v168, s[38:39]
	global_load_dwordx4 v[66:69], v168, s[38:39] offset:2048
	global_load_dwordx4 v[82:85], v168, s[40:41]
	global_load_dwordx4 v[58:61], v168, s[40:41] offset:2048
	s_waitcnt lgkmcnt(0)
	s_barrier
	v_add_u32_e32 v2, 0x2000, v172
	v_xor_b32_e32 v103, 64, v2
	v_mov_b32_e32 v2, 0
	v_xor_b32_e32 v104, 32, v171
	v_xor_b32_e32 v105, 64, v171
	v_xor_b32_e32 v106, 0x60, v171
	v_xor_b32_e32 v107, 0x80, v171
	v_xor_b32_e32 v108, 0xa0, v171
	v_xor_b32_e32 v109, 0xc0, v171
	s_add_i32 s72, s67, 0x2400
	v_xor_b32_e32 v110, 0xe0, v171
	s_add_i32 s73, s67, 0x2800
	s_add_i32 s74, s67, 0x2c00
	s_mov_b32 s52, 0
	s_mov_b64 s[48:49], 0
	v_mov_b32_e32 v3, v2
	v_mov_b32_e32 v4, v2
	v_mov_b32_e32 v5, v2
	v_mov_b32_e32 v10, v2
	v_mov_b32_e32 v11, v2
	v_mov_b32_e32 v12, v2
	v_mov_b32_e32 v13, v2
	v_mov_b32_e32 v14, v2
	v_mov_b32_e32 v15, v2
	v_mov_b32_e32 v16, v2
	v_mov_b32_e32 v17, v2
	v_mov_b32_e32 v30, v2
	v_mov_b32_e32 v31, v2
	v_mov_b32_e32 v32, v2
	v_mov_b32_e32 v33, v2
	v_mov_b32_e32 v34, v2
	v_mov_b32_e32 v35, v2
	v_mov_b32_e32 v36, v2
	v_mov_b32_e32 v37, v2
	v_mov_b32_e32 v62, v2
	v_mov_b32_e32 v63, v2
	v_mov_b32_e32 v64, v2
	v_mov_b32_e32 v65, v2
	v_mov_b32_e32 v54, v2
	v_mov_b32_e32 v55, v2
	v_mov_b32_e32 v56, v2
	v_mov_b32_e32 v57, v2
	v_mov_b32_e32 v86, v2
	v_mov_b32_e32 v87, v2
	v_mov_b32_e32 v88, v2
	v_mov_b32_e32 v89, v2
	v_mov_b32_e32 v6, v2
	v_mov_b32_e32 v7, v2
	v_mov_b32_e32 v8, v2
	v_mov_b32_e32 v9, v2
	v_mov_b32_e32 v42, v2
	v_mov_b32_e32 v43, v2
	v_mov_b32_e32 v44, v2
	v_mov_b32_e32 v45, v2
	v_mov_b32_e32 v18, v2
	v_mov_b32_e32 v19, v2
	v_mov_b32_e32 v20, v2
	v_mov_b32_e32 v21, v2
	v_mov_b32_e32 v70, v2
	v_mov_b32_e32 v71, v2
	v_mov_b32_e32 v72, v2
	v_mov_b32_e32 v73, v2
	v_mov_b32_e32 v46, v2
	v_mov_b32_e32 v47, v2
	v_mov_b32_e32 v48, v2
	v_mov_b32_e32 v49, v2
	v_mov_b32_e32 v90, v2
	v_mov_b32_e32 v91, v2
	v_mov_b32_e32 v92, v2
	v_mov_b32_e32 v93, v2
	v_mov_b32_e32 v74, v2
	v_mov_b32_e32 v75, v2
	v_mov_b32_e32 v76, v2
	v_mov_b32_e32 v77, v2
	v_mov_b32_e32 v94, v2
	v_mov_b32_e32 v95, v2
	v_mov_b32_e32 v96, v2
	v_mov_b32_e32 v97, v2

.LBB0_277:
	v_mov_b32_e32 v125, 0
	v_lshlrev_b32_e32 v98, 5, v134
	v_add_u32_e32 v99, 0x2000, v172
	s_andn2_b64 vcc, exec, s[10:11]
	v_xor_b32_e32 v178, 64, v172
	v_xor_b32_e32 v179, 32, v171
	v_xor_b32_e32 v180, 64, v171
	v_xor_b32_e32 v181, 0x60, v171
	v_xor_b32_e32 v182, 0x80, v171
	v_xor_b32_e32 v183, 0xa0, v171
	v_xor_b32_e32 v184, 0xc0, v171
	v_xor_b32_e32 v185, 0xe0, v171
	v_add_u32_e32 v186, v173, v98
	v_xor_b32_e32 v190, 32, v98
	v_xor_b32_e32 v189, 64, v98
	v_xor_b32_e32 v188, 0x60, v98
	v_xor_b32_e32 v187, 64, v99
	v_mov_b32_e32 v124, v125
	v_mov_b32_e32 v123, v125
	v_mov_b32_e32 v122, v125
	v_mov_b32_e32 v117, v125
	v_mov_b32_e32 v116, v125
	v_mov_b32_e32 v115, v125
	v_mov_b32_e32 v114, v125
	v_mov_b32_e32 v109, v125
	v_mov_b32_e32 v108, v125
	v_mov_b32_e32 v107, v125
	v_mov_b32_e32 v106, v125
	v_mov_b32_e32 v105, v125
	v_mov_b32_e32 v104, v125
	v_mov_b32_e32 v103, v125
	v_mov_b32_e32 v102, v125
	v_mov_b32_e32 v129, v125
	v_mov_b32_e32 v128, v125
	v_mov_b32_e32 v127, v125
	v_mov_b32_e32 v126, v125
	v_mov_b32_e32 v121, v125
	v_mov_b32_e32 v120, v125
	v_mov_b32_e32 v119, v125
	v_mov_b32_e32 v118, v125
	v_mov_b32_e32 v113, v125
	v_mov_b32_e32 v112, v125
	v_mov_b32_e32 v111, v125
	v_mov_b32_e32 v110, v125
	v_mov_b32_e32 v101, v125
	v_mov_b32_e32 v100, v125
	v_mov_b32_e32 v99, v125
	v_mov_b32_e32 v98, v125
	s_cbranch_vccnz .LBB0_281
	s_waitcnt vmcnt(9)
	v_lshlrev_b32_e32 v2, 8, v131
	v_and_or_b32 v191, v2, s60, v133
	s_waitcnt vmcnt(8)
	v_lshlrev_b32_e32 v2, 8, v130
	v_and_or_b32 v192, v2, s60, v132
	s_mov_b32 s6, m0
	s_mov_b32 m0, s67
	s_nop 0
	global_load_lds_dwordx4 v169, s[18:19]
	s_mov_b32 m0, s6
	s_add_i32 s50, s67, 0x800
	s_mov_b32 s6, m0
	s_mov_b32 m0, s68
	s_nop 0
	global_load_lds_dwordx4 v170, s[18:19]
	s_mov_b32 m0, s6
	s_add_i32 s51, s67, 0xc00
	s_mov_b32 s6, m0
	s_mov_b32 m0, s50
	s_nop 0
	global_load_lds_dwordx4 v174, s[18:19]
	s_mov_b32 m0, s6
	s_add_i32 s52, s67, 0x1000
	s_mov_b32 s6, m0
	s_mov_b32 m0, s51
	s_nop 0
	global_load_lds_dwordx4 v175, s[18:19]
	s_mov_b32 m0, s6
	s_add_i32 s53, s67, 0x1400
	s_mov_b32 s6, m0
	s_mov_b32 m0, s52
	s_nop 0
	global_load_lds_dwordx4 v176, s[18:19]
	s_mov_b32 m0, s6
	s_add_i32 s69, s67, 0x1800
	s_mov_b32 s6, m0
	s_mov_b32 m0, s53
	s_nop 0
	global_load_lds_dwordx4 v177, s[18:19]
	s_mov_b32 m0, s6
	s_add_i32 s70, s67, 0x1c00
	s_mov_b32 s6, m0
	s_mov_b32 m0, s69
	s_nop 0
	global_load_lds_dwordx4 v191, s[18:19]
	s_mov_b32 m0, s6
	v_add_u32_e32 v193, v173, v190
	s_mov_b32 s6, m0
	s_mov_b32 m0, s70
	s_nop 0
	global_load_lds_dwordx4 v192, s[18:19]
	s_mov_b32 m0, s6
	s_waitcnt vmcnt(8)
	v_mov_b32_e32 v138, v60
	v_mov_b32_e32 v139, v61
	v_mov_b32_e32 v140, v62
	v_mov_b32_e32 v141, v63
	v_mov_b32_e32 v134, v64
	v_mov_b32_e32 v135, v65
	v_mov_b32_e32 v136, v66
	v_mov_b32_e32 v137, v67
	v_mov_b32_e32 v142, v68
	v_mov_b32_e32 v143, v69
	v_mov_b32_e32 v144, v70
	v_mov_b32_e32 v145, v71
	v_mov_b32_e32 v130, v72
	v_mov_b32_e32 v131, v73
	v_mov_b32_e32 v132, v74
	v_mov_b32_e32 v133, v75
	v_add_u32_e32 v194, v173, v189
	v_cvt_pk_bf16_f32 v2, v228, v229
	v_cvt_pk_bf16_f32 v3, v230, v231
	ds_write_b64 v186, v[2:3]
	v_cvt_pk_bf16_f32 v2, v232, v233
	v_cvt_pk_bf16_f32 v3, v234, v235
	ds_write_b64 v193, v[2:3] offset:256
	v_cvt_pk_bf16_f32 v2, v236, v237
	v_cvt_pk_bf16_f32 v3, v238, v239
	ds_write_b64 v194, v[2:3] offset:512
	v_cvt_pk_bf16_f32 v2, v240, v241
	v_cvt_pk_bf16_f32 v3, v242, v243
	v_add_u32_e32 v195, v173, v188
	ds_write_b64 v195, v[2:3] offset:768
	global_load_dwordx4 v[154:157], v168, s[38:39]
	global_load_dwordx4 v[150:153], v168, s[38:39] offset:2048
	global_load_dwordx4 v[158:161], v168, s[40:41]
	global_load_dwordx4 v[146:149], v168, s[40:41] offset:2048
	s_waitcnt lgkmcnt(0)
	s_barrier
	v_mov_b32_e32 v98, 0
	s_add_i32 s71, s67, 0x2000
	s_add_i32 s72, s67, 0x2400
	s_add_i32 s73, s67, 0x2800
	s_add_i32 s74, s67, 0x2c00
	s_add_i32 s75, s67, 0x3000
	s_add_i32 s76, s67, 0x3400
	s_add_i32 s77, s67, 0x3800
	s_add_i32 s78, s67, 0x3c00
	s_mov_b32 s48, 0
	s_mov_b64 s[8:9], 0
	v_mov_b32_e32 v99, v98
	v_mov_b32_e32 v100, v98
	v_mov_b32_e32 v101, v98
	v_mov_b32_e32 v26, v98
	v_mov_b32_e32 v27, v98
	v_mov_b32_e32 v28, v98
	v_mov_b32_e32 v29, v98
	v_mov_b32_e32 v2, v98
	v_mov_b32_e32 v3, v98
	v_mov_b32_e32 v4, v98
	v_mov_b32_e32 v5, v98
	v_mov_b32_e32 v10, v98
	v_mov_b32_e32 v11, v98
	v_mov_b32_e32 v12, v98
	v_mov_b32_e32 v13, v98
	v_mov_b32_e32 v110, v98
	v_mov_b32_e32 v111, v98
	v_mov_b32_e32 v112, v98
	v_mov_b32_e32 v113, v98
	v_mov_b32_e32 v50, v98
	v_mov_b32_e32 v51, v98
	v_mov_b32_e32 v52, v98
	v_mov_b32_e32 v53, v98
	v_mov_b32_e32 v14, v98
	v_mov_b32_e32 v15, v98
	v_mov_b32_e32 v16, v98
	v_mov_b32_e32 v17, v98
	v_mov_b32_e32 v30, v98
	v_mov_b32_e32 v31, v98
	v_mov_b32_e32 v32, v98
	v_mov_b32_e32 v33, v98
	v_mov_b32_e32 v118, v98
	v_mov_b32_e32 v119, v98
	v_mov_b32_e32 v120, v98
	v_mov_b32_e32 v121, v98
	v_mov_b32_e32 v66, v98
	v_mov_b32_e32 v67, v98
	v_mov_b32_e32 v68, v98
	v_mov_b32_e32 v69, v98
	v_mov_b32_e32 v34, v98
	v_mov_b32_e32 v35, v98
	v_mov_b32_e32 v36, v98
	v_mov_b32_e32 v37, v98
	v_mov_b32_e32 v62, v98
	v_mov_b32_e32 v63, v98
	v_mov_b32_e32 v64, v98
	v_mov_b32_e32 v65, v98
	v_mov_b32_e32 v126, v98
	v_mov_b32_e32 v127, v98
	v_mov_b32_e32 v128, v98
	v_mov_b32_e32 v129, v98
	v_mov_b32_e32 v82, v98
	v_mov_b32_e32 v83, v98
	v_mov_b32_e32 v84, v98
	v_mov_b32_e32 v85, v98
	v_mov_b32_e32 v54, v98
	v_mov_b32_e32 v55, v98
	v_mov_b32_e32 v56, v98
	v_mov_b32_e32 v57, v98
	v_mov_b32_e32 v86, v98
	v_mov_b32_e32 v87, v98
	v_mov_b32_e32 v88, v98
	v_mov_b32_e32 v89, v98
	v_mov_b32_e32 v102, v98
	v_mov_b32_e32 v103, v98
	v_mov_b32_e32 v104, v98
	v_mov_b32_e32 v105, v98
	v_mov_b32_e32 v22, v98
	v_mov_b32_e32 v23, v98
	v_mov_b32_e32 v24, v98
	v_mov_b32_e32 v25, v98
	v_mov_b32_e32 v6, v98
	v_mov_b32_e32 v7, v98
	v_mov_b32_e32 v8, v98
	v_mov_b32_e32 v9, v98
	v_mov_b32_e32 v42, v98
	v_mov_b32_e32 v43, v98
	v_mov_b32_e32 v44, v98
	v_mov_b32_e32 v45, v98
	v_mov_b32_e32 v106, v98
	v_mov_b32_e32 v107, v98
	v_mov_b32_e32 v108, v98
	v_mov_b32_e32 v109, v98
	v_mov_b32_e32 v38, v98
	v_mov_b32_e32 v39, v98
	v_mov_b32_e32 v40, v98
	v_mov_b32_e32 v41, v98
	v_mov_b32_e32 v18, v98
	v_mov_b32_e32 v19, v98
	v_mov_b32_e32 v20, v98
	v_mov_b32_e32 v21, v98
	v_mov_b32_e32 v70, v98
	v_mov_b32_e32 v71, v98
	v_mov_b32_e32 v72, v98
	v_mov_b32_e32 v73, v98
	v_mov_b32_e32 v114, v98
	v_mov_b32_e32 v115, v98
	v_mov_b32_e32 v116, v98
	v_mov_b32_e32 v117, v98
	v_mov_b32_e32 v58, v98
	v_mov_b32_e32 v59, v98
	v_mov_b32_e32 v60, v98
	v_mov_b32_e32 v61, v98
	v_mov_b32_e32 v46, v98
	v_mov_b32_e32 v47, v98
	v_mov_b32_e32 v48, v98
	v_mov_b32_e32 v49, v98
	v_mov_b32_e32 v90, v98
	v_mov_b32_e32 v91, v98
	v_mov_b32_e32 v92, v98
	v_mov_b32_e32 v93, v98
	v_mov_b32_e32 v122, v98
	v_mov_b32_e32 v123, v98
	v_mov_b32_e32 v124, v98
	v_mov_b32_e32 v125, v98
	v_mov_b32_e32 v78, v98
	v_mov_b32_e32 v79, v98
	v_mov_b32_e32 v80, v98
	v_mov_b32_e32 v81, v98
	v_mov_b32_e32 v74, v98
	v_mov_b32_e32 v75, v98
	v_mov_b32_e32 v76, v98
	v_mov_b32_e32 v77, v98
	v_mov_b32_e32 v94, v98
	v_mov_b32_e32 v95, v98
	v_mov_b32_e32 v96, v98
	v_mov_b32_e32 v97, v98

.LBB0_281:
	s_and_b64 vcc, exec, s[8:9]
	s_cbranch_vccz .LBB0_285
	s_mov_b32 s6, m0
	s_mov_b32 m0, s67
	s_nop 0
	global_load_lds_dwordx4 v169, s[18:19]
	s_mov_b32 m0, s6
	v_add_u32_e32 v47, v173, v189
	s_mov_b32 s6, m0
	s_mov_b32 m0, s68
	s_nop 0
	global_load_lds_dwordx4 v170, s[18:19]
	s_mov_b32 m0, s6
	s_waitcnt vmcnt(2)
	v_mov_b32_e32 v18, v60
	v_mov_b32_e32 v19, v61
	v_mov_b32_e32 v20, v62
	v_mov_b32_e32 v21, v63
	v_mov_b32_e32 v6, v64
	v_mov_b32_e32 v7, v65
	v_mov_b32_e32 v8, v66
	v_mov_b32_e32 v9, v67
	v_mov_b32_e32 v14, v68
	v_mov_b32_e32 v15, v69
	v_mov_b32_e32 v16, v70
	v_mov_b32_e32 v17, v71
	v_mov_b32_e32 v2, v72
	v_mov_b32_e32 v3, v73
	v_mov_b32_e32 v4, v74
	v_mov_b32_e32 v5, v75
	v_add_u32_e32 v46, v173, v190
	v_cvt_pk_bf16_f32 v10, v228, v229
	v_cvt_pk_bf16_f32 v11, v230, v231
	ds_write_b64 v186, v[10:11]
	v_cvt_pk_bf16_f32 v10, v236, v237
	v_cvt_pk_bf16_f32 v11, v238, v239
	v_cvt_pk_bf16_f32 v12, v232, v233
	v_cvt_pk_bf16_f32 v13, v234, v235
	ds_write_b64 v47, v[10:11] offset:512
	v_cvt_pk_bf16_f32 v10, v240, v241
	v_cvt_pk_bf16_f32 v11, v242, v243
	v_add_u32_e32 v48, v173, v188
	ds_write_b64 v46, v[12:13] offset:256
	ds_write_b64 v48, v[10:11] offset:768
	global_load_dwordx4 v[38:41], v168, s[38:39]
	global_load_dwordx4 v[26:29], v168, s[38:39] offset:2048
	global_load_dwordx4 v[34:37], v168, s[40:41]
	global_load_dwordx4 v[22:25], v168, s[40:41] offset:2048
	s_waitcnt lgkmcnt(0)
	s_barrier
	v_mov_b32_e32 v10, 0
	s_add_i32 s48, s67, 0x2000
	s_add_i32 s49, s67, 0x2400
	s_mov_b32 s50, 0
	s_mov_b64 s[8:9], 0
	v_mov_b32_e32 v11, v10
	v_mov_b32_e32 v12, v10
	v_mov_b32_e32 v13, v10
	v_mov_b32_e32 v30, v10
	v_mov_b32_e32 v31, v10
	v_mov_b32_e32 v32, v10
	v_mov_b32_e32 v33, v10
	v_mov_b32_e32 v62, v10
	v_mov_b32_e32 v63, v10
	v_mov_b32_e32 v64, v10
	v_mov_b32_e32 v65, v10
	v_mov_b32_e32 v86, v10
	v_mov_b32_e32 v87, v10
	v_mov_b32_e32 v88, v10
	v_mov_b32_e32 v89, v10
	v_mov_b32_e32 v42, v10
	v_mov_b32_e32 v43, v10
	v_mov_b32_e32 v44, v10
	v_mov_b32_e32 v45, v10
	v_mov_b32_e32 v70, v10
	v_mov_b32_e32 v71, v10
	v_mov_b32_e32 v72, v10
	v_mov_b32_e32 v73, v10
	v_mov_b32_e32 v90, v10
	v_mov_b32_e32 v91, v10
	v_mov_b32_e32 v92, v10
	v_mov_b32_e32 v93, v10
	v_mov_b32_e32 v94, v10
	v_mov_b32_e32 v95, v10
	v_mov_b32_e32 v96, v10
	v_mov_b32_e32 v97, v10

.LBB0_869:
	s_sub_i32 s11, s62, s64
	v_mov_b32_e32 v162, v0
	s_min_i32 s11, s11, 0x200
	s_add_i32 s12, s11, 0x7f
	v_readfirstlane_b32 s10, v162
	s_lshr_b32 s66, s12, 7
	s_ashr_i32 s12, s10, 2
	s_and_b32 s12, s12, -16
	s_mul_i32 s12, s12, s66
	s_add_i32 s12, s12, s64
	v_bfe_u32 v2, v162, 3, 3
	v_or_b32_e32 v10, s12, v2
	s_add_i32 s65, s11, s64
	v_mov_b32_e32 v11, s64
	v_cmp_gt_i32_e32 vcc, s65, v10
	v_or_b32_e32 v4, 8, v10
	v_add_u32_e32 v6, 16, v10
	v_cndmask_b32_e32 v2, v11, v10, vcc
	v_cmp_gt_i32_e32 vcc, s65, v4
	s_cmpk_gt_u32 s11, 0x80
	s_cselect_b64 s[44:45], -1, 0
	v_cndmask_b32_e32 v4, v11, v4, vcc
	v_cmp_gt_i32_e32 vcc, s65, v6
	s_and_b64 vcc, s[44:45], vcc
	v_add_u32_e32 v8, 24, v10
	v_cndmask_b32_e32 v6, v11, v6, vcc
	v_cmp_gt_i32_e32 vcc, s65, v8
	s_and_b64 vcc, s[44:45], vcc
	v_ashrrev_i32_e32 v3, 31, v2
	v_ashrrev_i32_e32 v7, 31, v6
	v_cndmask_b32_e32 v8, v11, v8, vcc
	v_lshl_add_u64 v[2:3], v[2:3], 2, s[24:25]
	v_ashrrev_i32_e32 v5, 31, v4
	v_lshl_add_u64 v[6:7], v[6:7], 2, s[24:25]
	v_ashrrev_i32_e32 v9, 31, v8
	v_lshl_add_u64 v[4:5], v[4:5], 2, s[24:25]
	v_lshl_add_u64 v[8:9], v[8:9], 2, s[24:25]
	global_load_dword v12, v[2:3], off
	global_load_dword v13, v[4:5], off
	s_nop 0
	global_load_dword v6, v[6:7], off
	s_nop 0
	global_load_dword v7, v[8:9], off
	v_add_u32_e32 v2, 32, v10
	s_cmpk_gt_u32 s11, 0x100
	s_cselect_b64 s[42:43], -1, 0
	v_cmp_gt_i32_e32 vcc, s65, v2
	s_and_b64 vcc, s[42:43], vcc
	v_add_u32_e32 v4, 40, v10
	v_cndmask_b32_e32 v2, v11, v2, vcc
	v_cmp_gt_i32_e32 vcc, s65, v4
	s_and_b64 vcc, s[42:43], vcc
	v_ashrrev_i32_e32 v3, 31, v2
	v_cndmask_b32_e32 v4, v11, v4, vcc
	v_lshl_add_u64 v[2:3], v[2:3], 2, s[24:25]
	v_ashrrev_i32_e32 v5, 31, v4
	v_lshl_add_u64 v[4:5], v[4:5], 2, s[24:25]
	global_load_dword v8, v[2:3], off
	global_load_dword v9, v[4:5], off
	v_add_u32_e32 v2, 48, v10
	s_cmpk_gt_u32 s11, 0x180
	s_cselect_b64 s[40:41], -1, 0
	v_cmp_gt_i32_e32 vcc, s65, v2
	s_and_b64 vcc, s[40:41], vcc
	v_add_u32_e32 v4, 56, v10
	v_cndmask_b32_e32 v2, v11, v2, vcc
	v_cmp_gt_i32_e32 vcc, s65, v4
	s_and_b64 vcc, s[40:41], vcc
	v_ashrrev_i32_e32 v3, 31, v2
	v_cndmask_b32_e32 v4, v11, v4, vcc
	v_lshl_add_u64 v[2:3], v[2:3], 2, s[24:25]
	v_ashrrev_i32_e32 v5, 31, v4
	v_lshl_add_u64 v[4:5], v[4:5], 2, s[24:25]
	global_load_dword v131, v[2:3], off
	global_load_dword v130, v[4:5], off
	v_and_b32_e32 v10, 31, v162
	v_and_b32_e32 v2, 7, v162
	v_bfe_u32 v3, v162, 4, 2
	v_cmp_gt_u32_e32 vcc, 16, v10
	v_bitop3_b32 v2, v3, v2, 4 bitop3:0x36
	v_ashrrev_i32_e32 v11, 5, v162
	v_cndmask_b32_e32 v15, v166, v167, vcc
	v_bitop3_b32 v14, v3, v162, 7 bitop3:0x78
	v_lshlrev_b32_e32 v132, 4, v2
	v_lshl_add_u32 v2, v10, 4, v15
	v_lshlrev_b32_e32 v133, 4, v14
	v_lshl_or_b32 v168, v11, 13, v2
	global_load_dwordx4 v[228:231], v168, s[22:23]
	global_load_dwordx4 v[232:235], v168, s[22:23] offset:2048
	global_load_dwordx4 v[236:239], v168, s[28:29]
	global_load_dwordx4 v[240:243], v168, s[28:29] offset:2048
	global_load_dwordx4 v[60:63], v168, s[30:31]
	global_load_dwordx4 v[64:67], v168, s[30:31] offset:2048
	global_load_dwordx4 v[68:71], v168, s[34:35]
	global_load_dwordx4 v[72:75], v168, s[34:35] offset:2048
	v_lshrrev_b32_e32 v5, 4, v162
	v_lshlrev_b32_e32 v3, 11, v3
	s_lshl_b32 s10, s10, 8
	s_and_b32 s10, s10, 0xffffc000
	v_and_b32_e32 v4, 15, v162
	s_add_i32 s67, s10, 0
	s_add_i32 s68, s67, 0x400
	s_mov_b64 s[10:11], -1
	s_mov_b64 s[12:13], 0
	s_cmp_lt_i32 s66, 2
	s_mov_b64 s[14:15], 0
	s_waitcnt vmcnt(15)
	v_lshlrev_b32_e32 v2, 8, v12
	v_and_or_b32 v169, v2, s60, v133
	s_waitcnt vmcnt(14)
	v_lshlrev_b32_e32 v2, 8, v13
	v_and_or_b32 v170, v2, s60, v132
	s_waitcnt vmcnt(13)
	v_lshlrev_b32_e32 v2, 8, v6
	s_waitcnt vmcnt(12)
	v_lshlrev_b32_e32 v6, 8, v7
	v_and_or_b32 v175, v6, s60, v132
	v_and_or_b32 v174, v2, s60, v133
	s_waitcnt vmcnt(11)
	v_lshlrev_b32_e32 v2, 8, v8
	s_waitcnt vmcnt(10)
	v_lshlrev_b32_e32 v6, 8, v9
	v_and_or_b32 v177, v6, s60, v132
	v_lshlrev_b32_e32 v6, 3, v162
	v_and_or_b32 v176, v2, s60, v133
	v_lshlrev_b32_e32 v2, 10, v11
	v_and_b32_e32 v6, 24, v6
	v_add3_u32 v173, s61, v2, v6
	v_bfe_u32 v2, v162, 2, 3
	v_bitop3_b32 v134, v2, v5, 4 bitop3:0x78
	v_bfe_u32 v2, v162, 2, 2
	v_lshlrev_b32_e32 v7, 8, v2
	v_add3_u32 v3, s61, v3, v7
	v_lshrrev_b32_e32 v7, 2, v162
	v_and_or_b32 v2, v7, 4, v2
	v_lshlrev_b32_e32 v2, 5, v2
	v_add3_u32 v171, v3, v6, v2
	v_bfe_u32 v3, v162, 1, 3
	v_bitop3_b32 v3, v5, v3, 3 bitop3:0x6c
	v_lshlrev_b32_e32 v2, 7, v4
	v_lshlrev_b32_e32 v3, 4, v3
	v_add3_u32 v172, s67, v2, v3
	s_cbranch_scc1 .LBB0_881
	s_cmp_gt_i32 s66, 2
	s_cbranch_scc0 .LBB0_875
	s_cmp_eq_u32 s66, 3
	s_mov_b64 s[14:15], -1
	s_cbranch_scc0 .LBB0_876
	s_mov_b32 s10, m0
	s_mov_b32 m0, s67
	s_nop 0
	global_load_lds_dwordx4 v169, s[8:9]
	s_mov_b32 m0, s10
	s_add_i32 s50, s67, 0x800
	s_mov_b32 s10, m0
	s_mov_b32 m0, s68
	s_nop 0
	global_load_lds_dwordx4 v170, s[8:9]
	s_mov_b32 m0, s10
	s_add_i32 s51, s67, 0xc00
	s_mov_b32 s10, m0
	s_mov_b32 m0, s50
	s_nop 0
	global_load_lds_dwordx4 v174, s[8:9]
	s_mov_b32 m0, s10
	s_add_i32 s69, s67, 0x1000
	s_mov_b32 s10, m0
	s_mov_b32 m0, s51
	s_nop 0
	global_load_lds_dwordx4 v175, s[8:9]
	s_mov_b32 m0, s10
	s_add_i32 s70, s67, 0x1400
	s_mov_b32 s10, m0
	s_mov_b32 m0, s69
	s_nop 0
	global_load_lds_dwordx4 v176, s[8:9]
	s_mov_b32 m0, s10
	v_mov_b32_e32 v26, 0
	s_mov_b32 s10, m0
	s_mov_b32 m0, s70
	s_nop 0
	global_load_lds_dwordx4 v177, s[8:9]
	s_mov_b32 m0, s10
	s_waitcnt vmcnt(6)
	v_mov_b32_e32 v106, v60
	v_mov_b32_e32 v107, v61
	v_mov_b32_e32 v108, v62
	v_mov_b32_e32 v109, v63
	v_mov_b32_e32 v102, v64
	v_mov_b32_e32 v103, v65
	v_mov_b32_e32 v104, v66
	v_mov_b32_e32 v105, v67
	v_mov_b32_e32 v110, v68
	v_mov_b32_e32 v111, v69
	v_mov_b32_e32 v112, v70
	v_mov_b32_e32 v113, v71
	v_mov_b32_e32 v98, v72
	v_mov_b32_e32 v99, v73
	v_mov_b32_e32 v100, v74
	v_mov_b32_e32 v101, v75
	v_xor_b32_e32 v139, 64, v172
	v_cvt_pk_bf16_f32 v2, v228, v229
	v_cvt_pk_bf16_f32 v3, v230, v231
	v_lshlrev_b32_e32 v4, 5, v134
	v_add_u32_e32 v135, v173, v4
	v_xor_b32_e32 v5, 32, v4
	ds_write_b64 v135, v[2:3]
	v_cvt_pk_bf16_f32 v2, v232, v233
	v_cvt_pk_bf16_f32 v3, v234, v235
	v_add_u32_e32 v136, v173, v5
	v_xor_b32_e32 v5, 64, v4
	ds_write_b64 v136, v[2:3] offset:256
	v_cvt_pk_bf16_f32 v2, v236, v237
	v_cvt_pk_bf16_f32 v3, v238, v239
	v_add_u32_e32 v137, v173, v5
	v_xor_b32_e32 v4, 0x60, v4
	ds_write_b64 v137, v[2:3] offset:512
	v_cvt_pk_bf16_f32 v2, v240, v241
	v_cvt_pk_bf16_f32 v3, v242, v243
	v_add_u32_e32 v138, v173, v4
	ds_write_b64 v138, v[2:3] offset:768
	global_load_dwordx4 v[122:125], v168, s[36:37]
	global_load_dwordx4 v[118:121], v168, s[36:37] offset:2048
	global_load_dwordx4 v[126:129], v168, s[38:39]
	global_load_dwordx4 v[114:117], v168, s[38:39] offset:2048
	s_waitcnt lgkmcnt(0)
	s_barrier
	v_add_u32_e32 v2, 0x2000, v172
	s_add_i32 s71, s67, 0x2000
	v_xor_b32_e32 v140, 64, v2
	v_xor_b32_e32 v141, 32, v171
	v_xor_b32_e32 v142, 64, v171
	v_xor_b32_e32 v143, 0x60, v171
	v_xor_b32_e32 v144, 0x80, v171
	v_xor_b32_e32 v145, 0xa0, v171
	v_xor_b32_e32 v146, 0xc0, v171
	s_add_i32 s72, s67, 0x2400
	v_xor_b32_e32 v147, 0xe0, v171
	s_add_i32 s73, s67, 0x2800
	s_add_i32 s74, s67, 0x2c00
	s_add_i32 s75, s67, 0x3000
	s_add_i32 s76, s67, 0x3400
	s_mov_b32 s48, 0
	s_mov_b64 s[14:15], 0
	v_mov_b32_e32 v27, v26
	v_mov_b32_e32 v28, v26
	v_mov_b32_e32 v29, v26
	v_mov_b32_e32 v2, v26
	v_mov_b32_e32 v3, v26
	v_mov_b32_e32 v4, v26
	v_mov_b32_e32 v5, v26
	v_mov_b32_e32 v10, v26
	v_mov_b32_e32 v11, v26
	v_mov_b32_e32 v12, v26
	v_mov_b32_e32 v13, v26
	v_mov_b32_e32 v50, v26
	v_mov_b32_e32 v51, v26
	v_mov_b32_e32 v52, v26
	v_mov_b32_e32 v53, v26
	v_mov_b32_e32 v14, v26
	v_mov_b32_e32 v15, v26
	v_mov_b32_e32 v16, v26
	v_mov_b32_e32 v17, v26
	v_mov_b32_e32 v30, v26
	v_mov_b32_e32 v31, v26
	v_mov_b32_e32 v32, v26
	v_mov_b32_e32 v33, v26
	v_mov_b32_e32 v66, v26
	v_mov_b32_e32 v67, v26
	v_mov_b32_e32 v68, v26
	v_mov_b32_e32 v69, v26
	v_mov_b32_e32 v34, v26
	v_mov_b32_e32 v35, v26
	v_mov_b32_e32 v36, v26
	v_mov_b32_e32 v37, v26
	v_mov_b32_e32 v62, v26
	v_mov_b32_e32 v63, v26
	v_mov_b32_e32 v64, v26
	v_mov_b32_e32 v65, v26
	v_mov_b32_e32 v82, v26
	v_mov_b32_e32 v83, v26
	v_mov_b32_e32 v84, v26
	v_mov_b32_e32 v85, v26
	v_mov_b32_e32 v54, v26
	v_mov_b32_e32 v55, v26
	v_mov_b32_e32 v56, v26
	v_mov_b32_e32 v57, v26
	v_mov_b32_e32 v86, v26
	v_mov_b32_e32 v87, v26
	v_mov_b32_e32 v88, v26
	v_mov_b32_e32 v89, v26
	v_mov_b32_e32 v22, v26
	v_mov_b32_e32 v23, v26
	v_mov_b32_e32 v24, v26
	v_mov_b32_e32 v25, v26
	v_mov_b32_e32 v6, v26
	v_mov_b32_e32 v7, v26
	v_mov_b32_e32 v8, v26
	v_mov_b32_e32 v9, v26
	v_mov_b32_e32 v42, v26
	v_mov_b32_e32 v43, v26
	v_mov_b32_e32 v44, v26
	v_mov_b32_e32 v45, v26
	v_mov_b32_e32 v38, v26
	v_mov_b32_e32 v39, v26
	v_mov_b32_e32 v40, v26
	v_mov_b32_e32 v41, v26
	v_mov_b32_e32 v18, v26
	v_mov_b32_e32 v19, v26
	v_mov_b32_e32 v20, v26
	v_mov_b32_e32 v21, v26
	v_mov_b32_e32 v70, v26
	v_mov_b32_e32 v71, v26
	v_mov_b32_e32 v72, v26
	v_mov_b32_e32 v73, v26
	v_mov_b32_e32 v58, v26
	v_mov_b32_e32 v59, v26
	v_mov_b32_e32 v60, v26
	v_mov_b32_e32 v61, v26
	v_mov_b32_e32 v46, v26
	v_mov_b32_e32 v47, v26
	v_mov_b32_e32 v48, v26
	v_mov_b32_e32 v49, v26
	v_mov_b32_e32 v90, v26
	v_mov_b32_e32 v91, v26
	v_mov_b32_e32 v92, v26
	v_mov_b32_e32 v93, v26
	v_mov_b32_e32 v78, v26
	v_mov_b32_e32 v79, v26
	v_mov_b32_e32 v80, v26
	v_mov_b32_e32 v81, v26
	v_mov_b32_e32 v74, v26
	v_mov_b32_e32 v75, v26
	v_mov_b32_e32 v76, v26
	v_mov_b32_e32 v77, v26
	v_mov_b32_e32 v94, v26
	v_mov_b32_e32 v95, v26
	v_mov_b32_e32 v96, v26
	v_mov_b32_e32 v97, v26

.LBB0_877:
	s_mov_b32 s10, m0
	s_mov_b32 m0, s67
	s_nop 0
	global_load_lds_dwordx4 v169, s[8:9]
	s_mov_b32 m0, s10
	s_add_i32 s69, s67, 0x800
	s_mov_b32 s10, m0
	s_mov_b32 m0, s68
	s_nop 0
	global_load_lds_dwordx4 v170, s[8:9]
	s_mov_b32 m0, s10
	s_add_i32 s70, s67, 0xc00
	s_mov_b32 s10, m0
	s_mov_b32 m0, s69
	s_nop 0
	global_load_lds_dwordx4 v174, s[8:9]
	s_mov_b32 m0, s10
	v_xor_b32_e32 v102, 64, v172
	s_mov_b32 s10, m0
	s_mov_b32 m0, s70
	s_nop 0
	global_load_lds_dwordx4 v175, s[8:9]
	s_mov_b32 m0, s10
	s_waitcnt vmcnt(4)
	v_mov_b32_e32 v38, v60
	v_mov_b32_e32 v39, v61
	v_mov_b32_e32 v40, v62
	v_mov_b32_e32 v41, v63
	v_mov_b32_e32 v26, v64
	v_mov_b32_e32 v27, v65
	v_mov_b32_e32 v28, v66
	v_mov_b32_e32 v29, v67
	v_mov_b32_e32 v50, v68
	v_mov_b32_e32 v51, v69
	v_mov_b32_e32 v52, v70
	v_mov_b32_e32 v53, v71
	v_mov_b32_e32 v22, v72
	v_mov_b32_e32 v23, v73
	v_mov_b32_e32 v24, v74
	v_mov_b32_e32 v25, v75
	s_add_i32 s71, s67, 0x2000
	v_cvt_pk_bf16_f32 v2, v228, v229
	v_cvt_pk_bf16_f32 v3, v230, v231
	v_lshlrev_b32_e32 v4, 5, v134
	v_add_u32_e32 v98, v173, v4
	v_xor_b32_e32 v5, 32, v4
	ds_write_b64 v98, v[2:3]
	v_cvt_pk_bf16_f32 v2, v232, v233
	v_cvt_pk_bf16_f32 v3, v234, v235
	v_add_u32_e32 v99, v173, v5
	v_xor_b32_e32 v5, 64, v4
	ds_write_b64 v99, v[2:3] offset:256
	v_cvt_pk_bf16_f32 v2, v236, v237
	v_cvt_pk_bf16_f32 v3, v238, v239
	v_add_u32_e32 v100, v173, v5
	v_xor_b32_e32 v4, 0x60, v4
	ds_write_b64 v100, v[2:3] offset:512
	v_cvt_pk_bf16_f32 v2, v240, v241
	v_cvt_pk_bf16_f32 v3, v242, v243
	v_add_u32_e32 v101, v173, v4
	ds_write_b64 v101, v[2:3] offset:768
	global_load_dwordx4 v[78:81], v168, s[36:37]
	global_load_dwordx4 v[66:69], v168, s[36:37] offset:2048
	global_load_dwordx4 v[82:85], v168, s[38:39]
	global_load_dwordx4 v[58:61], v168, s[38:39] offset:2048
	s_waitcnt lgkmcnt(0)
	s_barrier
	v_add_u32_e32 v2, 0x2000, v172
	v_xor_b32_e32 v103, 64, v2
	v_mov_b32_e32 v2, 0
	v_xor_b32_e32 v104, 32, v171
	v_xor_b32_e32 v105, 64, v171
	v_xor_b32_e32 v106, 0x60, v171
	v_xor_b32_e32 v107, 0x80, v171
	v_xor_b32_e32 v108, 0xa0, v171
	v_xor_b32_e32 v109, 0xc0, v171
	s_add_i32 s72, s67, 0x2400
	v_xor_b32_e32 v110, 0xe0, v171
	s_add_i32 s73, s67, 0x2800
	s_add_i32 s74, s67, 0x2c00
	s_mov_b32 s50, 0
	s_mov_b64 s[46:47], 0
	v_mov_b32_e32 v3, v2
	v_mov_b32_e32 v4, v2
	v_mov_b32_e32 v5, v2
	v_mov_b32_e32 v10, v2
	v_mov_b32_e32 v11, v2
	v_mov_b32_e32 v12, v2
	v_mov_b32_e32 v13, v2
	v_mov_b32_e32 v14, v2
	v_mov_b32_e32 v15, v2
	v_mov_b32_e32 v16, v2
	v_mov_b32_e32 v17, v2
	v_mov_b32_e32 v30, v2
	v_mov_b32_e32 v31, v2
	v_mov_b32_e32 v32, v2
	v_mov_b32_e32 v33, v2
	v_mov_b32_e32 v34, v2
	v_mov_b32_e32 v35, v2
	v_mov_b32_e32 v36, v2
	v_mov_b32_e32 v37, v2
	v_mov_b32_e32 v62, v2
	v_mov_b32_e32 v63, v2
	v_mov_b32_e32 v64, v2
	v_mov_b32_e32 v65, v2
	v_mov_b32_e32 v54, v2
	v_mov_b32_e32 v55, v2
	v_mov_b32_e32 v56, v2
	v_mov_b32_e32 v57, v2
	v_mov_b32_e32 v86, v2
	v_mov_b32_e32 v87, v2
	v_mov_b32_e32 v88, v2
	v_mov_b32_e32 v89, v2
	v_mov_b32_e32 v6, v2
	v_mov_b32_e32 v7, v2
	v_mov_b32_e32 v8, v2
	v_mov_b32_e32 v9, v2
	v_mov_b32_e32 v42, v2
	v_mov_b32_e32 v43, v2
	v_mov_b32_e32 v44, v2
	v_mov_b32_e32 v45, v2
	v_mov_b32_e32 v18, v2
	v_mov_b32_e32 v19, v2
	v_mov_b32_e32 v20, v2
	v_mov_b32_e32 v21, v2
	v_mov_b32_e32 v70, v2
	v_mov_b32_e32 v71, v2
	v_mov_b32_e32 v72, v2
	v_mov_b32_e32 v73, v2
	v_mov_b32_e32 v46, v2
	v_mov_b32_e32 v47, v2
	v_mov_b32_e32 v48, v2
	v_mov_b32_e32 v49, v2
	v_mov_b32_e32 v90, v2
	v_mov_b32_e32 v91, v2
	v_mov_b32_e32 v92, v2
	v_mov_b32_e32 v93, v2
	v_mov_b32_e32 v74, v2
	v_mov_b32_e32 v75, v2
	v_mov_b32_e32 v76, v2
	v_mov_b32_e32 v77, v2
	v_mov_b32_e32 v94, v2
	v_mov_b32_e32 v95, v2
	v_mov_b32_e32 v96, v2
	v_mov_b32_e32 v97, v2

.LBB0_883:
	v_mov_b32_e32 v125, 0
	v_lshlrev_b32_e32 v98, 5, v134
	v_add_u32_e32 v99, 0x2000, v172
	s_andn2_b64 vcc, exec, s[14:15]
	v_xor_b32_e32 v178, 64, v172
	v_xor_b32_e32 v179, 32, v171
	v_xor_b32_e32 v180, 64, v171
	v_xor_b32_e32 v181, 0x60, v171
	v_xor_b32_e32 v182, 0x80, v171
	v_xor_b32_e32 v183, 0xa0, v171
	v_xor_b32_e32 v184, 0xc0, v171
	v_xor_b32_e32 v185, 0xe0, v171
	v_add_u32_e32 v186, v173, v98
	v_xor_b32_e32 v190, 32, v98
	v_xor_b32_e32 v189, 64, v98
	v_xor_b32_e32 v188, 0x60, v98
	v_xor_b32_e32 v187, 64, v99
	v_mov_b32_e32 v124, v125
	v_mov_b32_e32 v123, v125
	v_mov_b32_e32 v122, v125
	v_mov_b32_e32 v117, v125
	v_mov_b32_e32 v116, v125
	v_mov_b32_e32 v115, v125
	v_mov_b32_e32 v114, v125
	v_mov_b32_e32 v109, v125
	v_mov_b32_e32 v108, v125
	v_mov_b32_e32 v107, v125
	v_mov_b32_e32 v106, v125
	v_mov_b32_e32 v105, v125
	v_mov_b32_e32 v104, v125
	v_mov_b32_e32 v103, v125
	v_mov_b32_e32 v102, v125
	v_mov_b32_e32 v129, v125
	v_mov_b32_e32 v128, v125
	v_mov_b32_e32 v127, v125
	v_mov_b32_e32 v126, v125
	v_mov_b32_e32 v121, v125
	v_mov_b32_e32 v120, v125
	v_mov_b32_e32 v119, v125
	v_mov_b32_e32 v118, v125
	v_mov_b32_e32 v113, v125
	v_mov_b32_e32 v112, v125
	v_mov_b32_e32 v111, v125
	v_mov_b32_e32 v110, v125
	v_mov_b32_e32 v101, v125
	v_mov_b32_e32 v100, v125
	v_mov_b32_e32 v99, v125
	v_mov_b32_e32 v98, v125
	s_cbranch_vccnz .LBB0_887
	s_waitcnt vmcnt(9)
	v_lshlrev_b32_e32 v2, 8, v131
	v_and_or_b32 v191, v2, s60, v133
	s_waitcnt vmcnt(8)
	v_lshlrev_b32_e32 v2, 8, v130
	v_and_or_b32 v192, v2, s60, v132
	s_mov_b32 s10, m0
	s_mov_b32 m0, s67
	s_nop 0
	global_load_lds_dwordx4 v169, s[8:9]
	s_mov_b32 m0, s10
	s_add_i32 s48, s67, 0x800
	s_mov_b32 s10, m0
	s_mov_b32 m0, s68
	s_nop 0
	global_load_lds_dwordx4 v170, s[8:9]
	s_mov_b32 m0, s10
	s_add_i32 s49, s67, 0xc00
	s_mov_b32 s10, m0
	s_mov_b32 m0, s48
	s_nop 0
	global_load_lds_dwordx4 v174, s[8:9]
	s_mov_b32 m0, s10
	s_add_i32 s50, s67, 0x1000
	s_mov_b32 s10, m0
	s_mov_b32 m0, s49
	s_nop 0
	global_load_lds_dwordx4 v175, s[8:9]
	s_mov_b32 m0, s10
	s_add_i32 s51, s67, 0x1400
	s_mov_b32 s10, m0
	s_mov_b32 m0, s50
	s_nop 0
	global_load_lds_dwordx4 v176, s[8:9]
	s_mov_b32 m0, s10
	s_add_i32 s69, s67, 0x1800
	s_mov_b32 s10, m0
	s_mov_b32 m0, s51
	s_nop 0
	global_load_lds_dwordx4 v177, s[8:9]
	s_mov_b32 m0, s10
	s_add_i32 s70, s67, 0x1c00
	s_mov_b32 s10, m0
	s_mov_b32 m0, s69
	s_nop 0
	global_load_lds_dwordx4 v191, s[8:9]
	s_mov_b32 m0, s10
	v_add_u32_e32 v193, v173, v190
	s_mov_b32 s10, m0
	s_mov_b32 m0, s70
	s_nop 0
	global_load_lds_dwordx4 v192, s[8:9]
	s_mov_b32 m0, s10
	s_waitcnt vmcnt(8)
	v_mov_b32_e32 v138, v60
	v_mov_b32_e32 v139, v61
	v_mov_b32_e32 v140, v62
	v_mov_b32_e32 v141, v63
	v_mov_b32_e32 v134, v64
	v_mov_b32_e32 v135, v65
	v_mov_b32_e32 v136, v66
	v_mov_b32_e32 v137, v67
	v_mov_b32_e32 v142, v68
	v_mov_b32_e32 v143, v69
	v_mov_b32_e32 v144, v70
	v_mov_b32_e32 v145, v71
	v_mov_b32_e32 v130, v72
	v_mov_b32_e32 v131, v73
	v_mov_b32_e32 v132, v74
	v_mov_b32_e32 v133, v75
	v_add_u32_e32 v194, v173, v189
	v_cvt_pk_bf16_f32 v2, v228, v229
	v_cvt_pk_bf16_f32 v3, v230, v231
	ds_write_b64 v186, v[2:3]
	v_cvt_pk_bf16_f32 v2, v232, v233
	v_cvt_pk_bf16_f32 v3, v234, v235
	ds_write_b64 v193, v[2:3] offset:256
	v_cvt_pk_bf16_f32 v2, v236, v237
	v_cvt_pk_bf16_f32 v3, v238, v239
	ds_write_b64 v194, v[2:3] offset:512
	v_cvt_pk_bf16_f32 v2, v240, v241
	v_cvt_pk_bf16_f32 v3, v242, v243
	v_add_u32_e32 v195, v173, v188
	ds_write_b64 v195, v[2:3] offset:768
	global_load_dwordx4 v[154:157], v168, s[36:37]
	global_load_dwordx4 v[150:153], v168, s[36:37] offset:2048
	global_load_dwordx4 v[158:161], v168, s[38:39]
	global_load_dwordx4 v[146:149], v168, s[38:39] offset:2048
	s_waitcnt lgkmcnt(0)
	s_barrier
	v_mov_b32_e32 v98, 0
	s_add_i32 s71, s67, 0x2000
	s_add_i32 s72, s67, 0x2400
	s_add_i32 s73, s67, 0x2800
	s_add_i32 s74, s67, 0x2c00
	s_add_i32 s75, s67, 0x3000
	s_add_i32 s76, s67, 0x3400
	s_add_i32 s77, s67, 0x3800
	s_add_i32 s78, s67, 0x3c00
	s_mov_b32 s46, 0
	s_mov_b64 s[12:13], 0
	v_mov_b32_e32 v99, v98
	v_mov_b32_e32 v100, v98
	v_mov_b32_e32 v101, v98
	v_mov_b32_e32 v26, v98
	v_mov_b32_e32 v27, v98
	v_mov_b32_e32 v28, v98
	v_mov_b32_e32 v29, v98
	v_mov_b32_e32 v2, v98
	v_mov_b32_e32 v3, v98
	v_mov_b32_e32 v4, v98
	v_mov_b32_e32 v5, v98
	v_mov_b32_e32 v10, v98
	v_mov_b32_e32 v11, v98
	v_mov_b32_e32 v12, v98
	v_mov_b32_e32 v13, v98
	v_mov_b32_e32 v110, v98
	v_mov_b32_e32 v111, v98
	v_mov_b32_e32 v112, v98
	v_mov_b32_e32 v113, v98
	v_mov_b32_e32 v50, v98
	v_mov_b32_e32 v51, v98
	v_mov_b32_e32 v52, v98
	v_mov_b32_e32 v53, v98
	v_mov_b32_e32 v14, v98
	v_mov_b32_e32 v15, v98
	v_mov_b32_e32 v16, v98
	v_mov_b32_e32 v17, v98
	v_mov_b32_e32 v30, v98
	v_mov_b32_e32 v31, v98
	v_mov_b32_e32 v32, v98
	v_mov_b32_e32 v33, v98
	v_mov_b32_e32 v118, v98
	v_mov_b32_e32 v119, v98
	v_mov_b32_e32 v120, v98
	v_mov_b32_e32 v121, v98
	v_mov_b32_e32 v66, v98
	v_mov_b32_e32 v67, v98
	v_mov_b32_e32 v68, v98
	v_mov_b32_e32 v69, v98
	v_mov_b32_e32 v34, v98
	v_mov_b32_e32 v35, v98
	v_mov_b32_e32 v36, v98
	v_mov_b32_e32 v37, v98
	v_mov_b32_e32 v62, v98
	v_mov_b32_e32 v63, v98
	v_mov_b32_e32 v64, v98
	v_mov_b32_e32 v65, v98
	v_mov_b32_e32 v126, v98
	v_mov_b32_e32 v127, v98
	v_mov_b32_e32 v128, v98
	v_mov_b32_e32 v129, v98
	v_mov_b32_e32 v82, v98
	v_mov_b32_e32 v83, v98
	v_mov_b32_e32 v84, v98
	v_mov_b32_e32 v85, v98
	v_mov_b32_e32 v54, v98
	v_mov_b32_e32 v55, v98
	v_mov_b32_e32 v56, v98
	v_mov_b32_e32 v57, v98
	v_mov_b32_e32 v86, v98
	v_mov_b32_e32 v87, v98
	v_mov_b32_e32 v88, v98
	v_mov_b32_e32 v89, v98
	v_mov_b32_e32 v102, v98
	v_mov_b32_e32 v103, v98
	v_mov_b32_e32 v104, v98
	v_mov_b32_e32 v105, v98
	v_mov_b32_e32 v22, v98
	v_mov_b32_e32 v23, v98
	v_mov_b32_e32 v24, v98
	v_mov_b32_e32 v25, v98
	v_mov_b32_e32 v6, v98
	v_mov_b32_e32 v7, v98
	v_mov_b32_e32 v8, v98
	v_mov_b32_e32 v9, v98
	v_mov_b32_e32 v42, v98
	v_mov_b32_e32 v43, v98
	v_mov_b32_e32 v44, v98
	v_mov_b32_e32 v45, v98
	v_mov_b32_e32 v106, v98
	v_mov_b32_e32 v107, v98
	v_mov_b32_e32 v108, v98
	v_mov_b32_e32 v109, v98
	v_mov_b32_e32 v38, v98
	v_mov_b32_e32 v39, v98
	v_mov_b32_e32 v40, v98
	v_mov_b32_e32 v41, v98
	v_mov_b32_e32 v18, v98
	v_mov_b32_e32 v19, v98
	v_mov_b32_e32 v20, v98
	v_mov_b32_e32 v21, v98
	v_mov_b32_e32 v70, v98
	v_mov_b32_e32 v71, v98
	v_mov_b32_e32 v72, v98
	v_mov_b32_e32 v73, v98
	v_mov_b32_e32 v114, v98
	v_mov_b32_e32 v115, v98
	v_mov_b32_e32 v116, v98
	v_mov_b32_e32 v117, v98
	v_mov_b32_e32 v58, v98
	v_mov_b32_e32 v59, v98
	v_mov_b32_e32 v60, v98
	v_mov_b32_e32 v61, v98
	v_mov_b32_e32 v46, v98
	v_mov_b32_e32 v47, v98
	v_mov_b32_e32 v48, v98
	v_mov_b32_e32 v49, v98
	v_mov_b32_e32 v90, v98
	v_mov_b32_e32 v91, v98
	v_mov_b32_e32 v92, v98
	v_mov_b32_e32 v93, v98
	v_mov_b32_e32 v122, v98
	v_mov_b32_e32 v123, v98
	v_mov_b32_e32 v124, v98
	v_mov_b32_e32 v125, v98
	v_mov_b32_e32 v78, v98
	v_mov_b32_e32 v79, v98
	v_mov_b32_e32 v80, v98
	v_mov_b32_e32 v81, v98
	v_mov_b32_e32 v74, v98
	v_mov_b32_e32 v75, v98
	v_mov_b32_e32 v76, v98
	v_mov_b32_e32 v77, v98
	v_mov_b32_e32 v94, v98
	v_mov_b32_e32 v95, v98
	v_mov_b32_e32 v96, v98
	v_mov_b32_e32 v97, v98

.LBB0_887:
	s_and_b64 vcc, exec, s[12:13]
	s_cbranch_vccz .LBB0_891
	s_mov_b32 s10, m0
	s_mov_b32 m0, s67
	s_nop 0
	global_load_lds_dwordx4 v169, s[8:9]
	s_mov_b32 m0, s10
	v_add_u32_e32 v47, v173, v189
	s_mov_b32 s10, m0
	s_mov_b32 m0, s68
	s_nop 0
	global_load_lds_dwordx4 v170, s[8:9]
	s_mov_b32 m0, s10
	s_waitcnt vmcnt(2)
	v_mov_b32_e32 v18, v60
	v_mov_b32_e32 v19, v61
	v_mov_b32_e32 v20, v62
	v_mov_b32_e32 v21, v63
	v_mov_b32_e32 v6, v64
	v_mov_b32_e32 v7, v65
	v_mov_b32_e32 v8, v66
	v_mov_b32_e32 v9, v67
	v_mov_b32_e32 v14, v68
	v_mov_b32_e32 v15, v69
	v_mov_b32_e32 v16, v70
	v_mov_b32_e32 v17, v71
	v_mov_b32_e32 v2, v72
	v_mov_b32_e32 v3, v73
	v_mov_b32_e32 v4, v74
	v_mov_b32_e32 v5, v75
	v_add_u32_e32 v46, v173, v190
	v_cvt_pk_bf16_f32 v10, v228, v229
	v_cvt_pk_bf16_f32 v11, v230, v231
	ds_write_b64 v186, v[10:11]
	v_cvt_pk_bf16_f32 v10, v236, v237
	v_cvt_pk_bf16_f32 v11, v238, v239
	v_cvt_pk_bf16_f32 v12, v232, v233
	v_cvt_pk_bf16_f32 v13, v234, v235
	ds_write_b64 v47, v[10:11] offset:512
	v_cvt_pk_bf16_f32 v10, v240, v241
	v_cvt_pk_bf16_f32 v11, v242, v243
	v_add_u32_e32 v48, v173, v188
	ds_write_b64 v46, v[12:13] offset:256
	ds_write_b64 v48, v[10:11] offset:768
	global_load_dwordx4 v[38:41], v168, s[36:37]
	global_load_dwordx4 v[26:29], v168, s[36:37] offset:2048
	global_load_dwordx4 v[34:37], v168, s[38:39]
	global_load_dwordx4 v[22:25], v168, s[38:39] offset:2048
	s_waitcnt lgkmcnt(0)
	s_barrier
	v_mov_b32_e32 v10, 0
	s_add_i32 s46, s67, 0x2000
	s_add_i32 s47, s67, 0x2400
	s_mov_b32 s48, 0
	s_mov_b64 s[12:13], 0
	v_mov_b32_e32 v11, v10
	v_mov_b32_e32 v12, v10
	v_mov_b32_e32 v13, v10
	v_mov_b32_e32 v30, v10
	v_mov_b32_e32 v31, v10
	v_mov_b32_e32 v32, v10
	v_mov_b32_e32 v33, v10
	v_mov_b32_e32 v62, v10
	v_mov_b32_e32 v63, v10
	v_mov_b32_e32 v64, v10
	v_mov_b32_e32 v65, v10
	v_mov_b32_e32 v86, v10
	v_mov_b32_e32 v87, v10
	v_mov_b32_e32 v88, v10
	v_mov_b32_e32 v89, v10
	v_mov_b32_e32 v42, v10
	v_mov_b32_e32 v43, v10
	v_mov_b32_e32 v44, v10
	v_mov_b32_e32 v45, v10
	v_mov_b32_e32 v70, v10
	v_mov_b32_e32 v71, v10
	v_mov_b32_e32 v72, v10
	v_mov_b32_e32 v73, v10
	v_mov_b32_e32 v90, v10
	v_mov_b32_e32 v91, v10
	v_mov_b32_e32 v92, v10
	v_mov_b32_e32 v93, v10
	v_mov_b32_e32 v94, v10
	v_mov_b32_e32 v95, v10
	v_mov_b32_e32 v96, v10
	v_mov_b32_e32 v97, v10
